# band attention: second QK accumulator takes the bias constant registers as srcC directly (8 v_mov_b64 per step removed)
# speedup vs baseline: 1.0020x; 1.0020x over previous
; #define LAS __attribute__((address_space(3)))
; #define MFMA32(a, b, c) __builtin_amdgcn_mfma_f32_32x32x16_bf16((a), (b), (c), 0, 0, 0)
; __device__ __forceinline__ void unit(LAS unsigned char* lds, const bf16* __restrict__ Q, const bf16* __restrict__ Kp, const bf16* __restrict__ VT, const float* __restrict__ rel, bf16* mix, float* ssa, int b, int h, int u) {
;     ...
;             bf16x8 kf0[4], kf1[4], vf0[4], vf1[4];
; #pragma unroll
;             for (int d0 = 0; d0 < 4; ++d0) { const LAS unsigned char* kp_ = lds + (kof[d0] + sbo); kf0[d0] = *(const LAS bf16x8*)kp_; kf1[d0] = *(const LAS bf16x8*)(kp_ + 4096); }
; #pragma unroll
;             for (int d0 = 0; d0 < 4; ++d0) { const LAS unsigned char* vp_ = lds + (vof[d0] + sbo); vf0[d0] = *(const LAS bf16x8*)vp_; vf1[d0] = *(const LAS bf16x8*)(vp_ + 4096); }
;             f32x16 p0 = MFMA32(kf0[0], qf[0], cfarv), p1 = MFMA32(kf1[0], qf[0], cfarv);
; #pragma unroll
;             for (int d0 = 1; d0 < 4; ++d0) { p0 = MFMA32(kf0[d0], qf[d0], p0); p1 = MFMA32(kf1[d0], qf[d0], p1); }
;             if (dj < 3) { const LAS float* tb = tab + (64 * dj + 32 * qh + r32 + 128 - 8 * hh - 55); asm volatile("" : "+v"(tb));
; #pragma unroll
;                 for (int r = 0; r < 16; ++r) { p0[r] += tb[55 - (16 * (r >> 3) + (r & 7))]; p1[r] += tb[23 - (16 * (r >> 3) + (r & 7))]; } }
.LBB5_985:
	s_add_i32 s36, s54, s55
	s_cmp_lt_i32 s36, 0
	s_cbranch_scc1 .LBB5_996
	s_mul_hi_u32 s36, s52, 0xaaaaaaab
	s_lshr_b32 s36, s36, 2
	s_mul_i32 s36, s36, 0x18000
	s_sub_i32 s36, s53, s36
	s_add_i32 s36, s36, 0
	v_add_u32_e32 v2, s36, v182
	ds_read_b128 v[4:7], v2
	ds_read_b128 v[8:11], v2 offset:4096
	s_waitcnt lgkmcnt(0)
	v_mfma_f32_32x32x16_bf16 v[98:113], v[4:7], v[118:121], v[66:81]
	v_add_u32_e32 v2, s36, v184
	s_cmp_lt_u32 s55, 6
	v_mfma_f32_32x32x16_bf16 v[82:97], v[8:11], v[118:121], v[66:81]
	ds_read_b128 v[4:7], v2
	ds_read_b128 v[8:11], v2 offset:4096
	v_add_u32_e32 v2, s36, v186
	s_waitcnt lgkmcnt(0)
	v_mfma_f32_32x32x16_bf16 v[98:113], v[4:7], v[122:125], v[98:113]
	v_mfma_f32_32x32x16_bf16 v[82:97], v[8:11], v[122:125], v[82:97]
	ds_read_b128 v[4:7], v2
	ds_read_b128 v[8:11], v2 offset:4096
	v_add_u32_e32 v2, s36, v188
	ds_read_b128 v[12:15], v2
	ds_read_b128 v[192:195], v2 offset:4096
	v_add_u32_e32 v2, s36, v183
	s_waitcnt lgkmcnt(0)
	v_mfma_f32_32x32x16_bf16 v[98:113], v[4:7], v[126:129], v[98:113]
	ds_read_b128 v[150:153], v2
	ds_read_b128 v[4:7], v2 offset:4096
	v_add_u32_e32 v2, s36, v185
	v_mfma_f32_32x32x16_bf16 v[82:97], v[8:11], v[126:129], v[82:97]
	ds_read_b128 v[146:149], v2
	ds_read_b128 v[8:11], v2 offset:4096
	v_add_u32_e32 v2, s36, v187
	v_mfma_f32_32x32x16_bf16 v[98:113], v[12:15], v[130:133], v[98:113]
	ds_read_b128 v[142:145], v2
	ds_read_b128 v[12:15], v2 offset:4096
	v_add_u32_e32 v2, s36, v189
	ds_read_b128 v[138:141], v2
	ds_read_b128 v[134:137], v2 offset:4096
	v_mfma_f32_32x32x16_bf16 v[82:97], v[192:195], v[130:133], v[82:97]
	s_cbranch_scc1 .LBB5_988
	v_mov_b32_e32 v2, v190
	ds_read2_b32 v[16:17], v2 offset0:54 offset1:55
	ds_read2_b32 v[192:193], v2 offset0:22 offset1:23
	ds_read2_b32 v[194:195], v2 offset0:52 offset1:53
	ds_read2_b32 v[196:197], v2 offset0:20 offset1:21
	s_waitcnt lgkmcnt(0)
	v_pk_add_f32 v[98:99], v[98:99], v[16:17] op_sel:[0,1] op_sel_hi:[1,0]
	ds_read2_b32 v[16:17], v2 offset0:50 offset1:51
	s_nop 2
	v_pk_add_f32 v[82:83], v[82:83], v[192:193] op_sel:[0,1] op_sel_hi:[1,0]
	v_pk_add_f32 v[100:101], v[100:101], v[194:195] op_sel:[0,1] op_sel_hi:[1,0]
	ds_read2_b32 v[192:193], v2 offset0:18 offset1:19
	ds_read2_b32 v[194:195], v2 offset0:48 offset1:49
	s_waitcnt lgkmcnt(0)
	v_pk_add_f32 v[102:103], v[102:103], v[16:17] op_sel:[0,1] op_sel_hi:[1,0]
	ds_read2_b32 v[16:17], v2 offset0:16 offset1:17
	v_pk_add_f32 v[84:85], v[84:85], v[196:197] op_sel:[0,1] op_sel_hi:[1,0]
	v_pk_add_f32 v[86:87], v[86:87], v[192:193] op_sel:[0,1] op_sel_hi:[1,0]
	ds_read2_b32 v[192:193], v2 offset0:38 offset1:39
	v_pk_add_f32 v[104:105], v[104:105], v[194:195] op_sel:[0,1] op_sel_hi:[1,0]
	ds_read2_b32 v[194:195], v2 offset0:6 offset1:7
	s_waitcnt lgkmcnt(0)
	v_pk_add_f32 v[88:89], v[88:89], v[16:17] op_sel:[0,1] op_sel_hi:[1,0]
	ds_read2_b32 v[16:17], v2 offset0:36 offset1:37
	v_pk_add_f32 v[106:107], v[106:107], v[192:193] op_sel:[0,1] op_sel_hi:[1,0]
	ds_read2_b32 v[192:193], v2 offset0:4 offset1:5
	v_pk_add_f32 v[90:91], v[90:91], v[194:195] op_sel:[0,1] op_sel_hi:[1,0]
	ds_read2_b32 v[194:195], v2 offset0:34 offset1:35
	s_waitcnt lgkmcnt(0)
	v_pk_add_f32 v[108:109], v[108:109], v[16:17] op_sel:[0,1] op_sel_hi:[1,0]
	ds_read2_b32 v[16:17], v2 offset0:2 offset1:3
	ds_read2_b32 v[196:197], v2 offset0:32 offset1:33
	ds_read2_b32 v[200:201], v2 offset1:1
	v_pk_add_f32 v[92:93], v[92:93], v[192:193] op_sel:[0,1] op_sel_hi:[1,0]
	v_pk_add_f32 v[110:111], v[110:111], v[194:195] op_sel:[0,1] op_sel_hi:[1,0]
	s_waitcnt lgkmcnt(0)
	v_pk_add_f32 v[94:95], v[94:95], v[16:17] op_sel:[0,1] op_sel_hi:[1,0]
	v_pk_add_f32 v[112:113], v[112:113], v[196:197] op_sel:[0,1] op_sel_hi:[1,0]
	v_pk_add_f32 v[96:97], v[96:97], v[200:201] op_sel:[0,1] op_sel_hi:[1,0]

; #define LAS __attribute__((address_space(3)))
; #define MFMA32(a, b, c) __builtin_amdgcn_mfma_f32_32x32x16_bf16((a), (b), (c), 0, 0, 0)
; __device__ __forceinline__ void unit(LAS unsigned char* lds, const bf16* __restrict__ Q, const bf16* __restrict__ Kp, const bf16* __restrict__ VT, const float* __restrict__ rel, bf16* mix, float* ssa, int b, int h, int u) {
;     ...
;             bf16x8 kf0[4], kf1[4], vf0[4], vf1[4];
; #pragma unroll
;             for (int d0 = 0; d0 < 4; ++d0) { const LAS unsigned char* kp_ = lds + (kof[d0] + sbo); kf0[d0] = *(const LAS bf16x8*)kp_; kf1[d0] = *(const LAS bf16x8*)(kp_ + 4096); }
; #pragma unroll
;             for (int d0 = 0; d0 < 4; ++d0) { const LAS unsigned char* vp_ = lds + (vof[d0] + sbo); vf0[d0] = *(const LAS bf16x8*)vp_; vf1[d0] = *(const LAS bf16x8*)(vp_ + 4096); }
;             f32x16 p0 = MFMA32(kf0[0], qf[0], cfarv), p1 = MFMA32(kf1[0], qf[0], cfarv);
; #pragma unroll
;             for (int d0 = 1; d0 < 4; ++d0) { p0 = MFMA32(kf0[d0], qf[d0], p0); p1 = MFMA32(kf1[d0], qf[d0], p1); }
;             if (dj < 3) { const LAS float* tb = tab + (64 * dj + 32 * qh + r32 + 128 - 8 * hh - 55); asm volatile("" : "+v"(tb));
; #pragma unroll
;                 for (int r = 0; r < 16; ++r) { p0[r] += tb[55 - (16 * (r >> 3) + (r & 7))]; p1[r] += tb[23 - (16 * (r >> 3) + (r & 7))]; } }
.LBB5_1021:
	s_add_i32 s34, s53, s54
	s_cmp_lt_i32 s34, 0
	s_cbranch_scc1 .LBB5_1032
	s_mul_hi_u32 s34, s51, 0xaaaaaaab
	s_lshr_b32 s34, s34, 2
	s_mul_i32 s34, s34, 0x18000
	s_sub_i32 s34, s52, s34
	s_add_i32 s34, s34, 0
	v_add_u32_e32 v2, s34, v180
	ds_read_b128 v[4:7], v2
	ds_read_b128 v[8:11], v2 offset:4096
	s_waitcnt lgkmcnt(0)
	v_mfma_f32_32x32x16_bf16 v[98:113], v[4:7], v[118:121], v[66:81]
	v_add_u32_e32 v2, s34, v182
	s_cmp_lt_u32 s54, 6
	v_mfma_f32_32x32x16_bf16 v[82:97], v[8:11], v[118:121], v[66:81]
	ds_read_b128 v[4:7], v2
	ds_read_b128 v[8:11], v2 offset:4096
	v_add_u32_e32 v2, s34, v184
	s_waitcnt lgkmcnt(0)
	v_mfma_f32_32x32x16_bf16 v[98:113], v[4:7], v[122:125], v[98:113]
	v_mfma_f32_32x32x16_bf16 v[82:97], v[8:11], v[122:125], v[82:97]
	ds_read_b128 v[4:7], v2
	ds_read_b128 v[8:11], v2 offset:4096
	v_add_u32_e32 v2, s34, v186
	ds_read_b128 v[12:15], v2
	ds_read_b128 v[190:193], v2 offset:4096
	v_add_u32_e32 v2, s34, v179
	s_waitcnt lgkmcnt(0)
	v_mfma_f32_32x32x16_bf16 v[98:113], v[4:7], v[126:129], v[98:113]
	ds_read_b128 v[150:153], v2
	ds_read_b128 v[4:7], v2 offset:4096
	v_add_u32_e32 v2, s34, v181
	v_mfma_f32_32x32x16_bf16 v[82:97], v[8:11], v[126:129], v[82:97]
	ds_read_b128 v[146:149], v2
	ds_read_b128 v[8:11], v2 offset:4096
	v_add_u32_e32 v2, s34, v183
	v_mfma_f32_32x32x16_bf16 v[98:113], v[12:15], v[130:133], v[98:113]
	ds_read_b128 v[142:145], v2
	ds_read_b128 v[12:15], v2 offset:4096
	v_add_u32_e32 v2, s34, v185
	ds_read_b128 v[138:141], v2
	ds_read_b128 v[134:137], v2 offset:4096
	v_mfma_f32_32x32x16_bf16 v[82:97], v[190:193], v[130:133], v[82:97]
	s_cbranch_scc1 .LBB5_1024
	v_mov_b32_e32 v2, v187
	ds_read2_b32 v[16:17], v2 offset0:54 offset1:55
	ds_read2_b32 v[190:191], v2 offset0:22 offset1:23
	ds_read2_b32 v[192:193], v2 offset0:52 offset1:53
	ds_read2_b32 v[194:195], v2 offset0:20 offset1:21
	s_waitcnt lgkmcnt(0)
	v_pk_add_f32 v[98:99], v[98:99], v[16:17] op_sel:[0,1] op_sel_hi:[1,0]
	ds_read2_b32 v[16:17], v2 offset0:50 offset1:51
	s_nop 2
	v_pk_add_f32 v[82:83], v[82:83], v[190:191] op_sel:[0,1] op_sel_hi:[1,0]
	v_pk_add_f32 v[100:101], v[100:101], v[192:193] op_sel:[0,1] op_sel_hi:[1,0]
	ds_read2_b32 v[190:191], v2 offset0:18 offset1:19
	ds_read2_b32 v[192:193], v2 offset0:48 offset1:49
	s_waitcnt lgkmcnt(0)
	v_pk_add_f32 v[102:103], v[102:103], v[16:17] op_sel:[0,1] op_sel_hi:[1,0]
	ds_read2_b32 v[16:17], v2 offset0:16 offset1:17
	v_pk_add_f32 v[84:85], v[84:85], v[194:195] op_sel:[0,1] op_sel_hi:[1,0]
	v_pk_add_f32 v[86:87], v[86:87], v[190:191] op_sel:[0,1] op_sel_hi:[1,0]
	ds_read2_b32 v[190:191], v2 offset0:38 offset1:39
	v_pk_add_f32 v[104:105], v[104:105], v[192:193] op_sel:[0,1] op_sel_hi:[1,0]
	ds_read2_b32 v[192:193], v2 offset0:6 offset1:7
	s_waitcnt lgkmcnt(0)
	v_pk_add_f32 v[88:89], v[88:89], v[16:17] op_sel:[0,1] op_sel_hi:[1,0]
	ds_read2_b32 v[16:17], v2 offset0:36 offset1:37
	v_pk_add_f32 v[106:107], v[106:107], v[190:191] op_sel:[0,1] op_sel_hi:[1,0]
	ds_read2_b32 v[190:191], v2 offset0:4 offset1:5
	v_pk_add_f32 v[90:91], v[90:91], v[192:193] op_sel:[0,1] op_sel_hi:[1,0]
	ds_read2_b32 v[192:193], v2 offset0:34 offset1:35
	s_waitcnt lgkmcnt(0)
	v_pk_add_f32 v[108:109], v[108:109], v[16:17] op_sel:[0,1] op_sel_hi:[1,0]
	ds_read2_b32 v[16:17], v2 offset0:2 offset1:3
	ds_read2_b32 v[194:195], v2 offset0:32 offset1:33
	ds_read2_b32 v[196:197], v2 offset1:1
	v_pk_add_f32 v[92:93], v[92:93], v[190:191] op_sel:[0,1] op_sel_hi:[1,0]
	v_pk_add_f32 v[110:111], v[110:111], v[192:193] op_sel:[0,1] op_sel_hi:[1,0]
	s_waitcnt lgkmcnt(0)
	v_pk_add_f32 v[94:95], v[94:95], v[16:17] op_sel:[0,1] op_sel_hi:[1,0]
	v_pk_add_f32 v[112:113], v[112:113], v[194:195] op_sel:[0,1] op_sel_hi:[1,0]
	v_pk_add_f32 v[96:97], v[96:97], v[196:197] op_sel:[0,1] op_sel_hi:[1,0]
